# expert weight conversion hosted in the grid barriers: waves 1-7 two tiles per barrier (all of their tiles), wave 0 in the attention phase
# speedup vs baseline: 1.0643x; 1.0092x over previous
.LBB0_258:
	s_cmp_lg_u32 s35, 0
	s_cselect_b64 s[66:67], -1, 0
	s_min_i32 s0, s3, 4
	s_add_i32 s2, s0, s20
	s_cmp_eq_u32 s35, 0
	s_cselect_b64 s[86:87], -1, 0
	s_and_b64 s[0:1], s[86:87], exec
	s_cselect_b32 s0, s2, 8
	s_mov_b32 s99, 0
	s_cmp_gt_u32 s98, 26623
	s_cbranch_scc1 .Lhw_x_skip
	s_sub_i32 s23, s98, 2048
	s_and_b32 s32, s23, 7
	s_cmp_eq_u32 s32, 0
	s_cbranch_scc1 .Lhw_x_go
	s_lshr_b32 s32, s23, 11
	s_cmp_lt_u32 s32, 4
	s_cbranch_scc0 .Lhw_x_skip

.Lhw_go_s0_0:
	s_add_u32 s100, s82, s69
	s_addc_u32 s101, s83, 0
	v_readlane_b32 s82, v239, 44
	v_readlane_b32 s83, v239, 45
	s_add_u32 s82, s82, s99
	s_addc_u32 s83, s83, 0
	global_load_dword v34, v178, s[100:101] nt
	s_add_u32 s100, s100, s89
	s_addc_u32 s101, s101, 0
	global_load_dword v35, v178, s[100:101] nt
	s_add_u32 s100, s100, s89
	s_addc_u32 s101, s101, 0
	global_load_dword v36, v178, s[100:101] nt
	s_add_u32 s100, s100, s89
	s_addc_u32 s101, s101, 0
	global_load_dword v37, v178, s[100:101] nt
	s_add_u32 s100, s100, s89
	s_addc_u32 s101, s101, 0
	global_load_dword v38, v178, s[100:101] nt
	s_add_u32 s100, s100, s89
	s_addc_u32 s101, s101, 0
	global_load_dword v39, v178, s[100:101] nt
	s_add_u32 s100, s100, s89
	s_addc_u32 s101, s101, 0
	global_load_dword v40, v178, s[100:101] nt
	s_add_u32 s100, s100, s89
	s_addc_u32 s101, s101, 0
	global_load_dword v41, v178, s[100:101] nt
	s_add_u32 s100, s100, s89
	s_addc_u32 s101, s101, 0
	global_load_dword v42, v178, s[100:101] nt
	s_add_u32 s100, s100, s89
	s_addc_u32 s101, s101, 0
	global_load_dword v43, v178, s[100:101] nt
	s_add_u32 s100, s100, s89
	s_addc_u32 s101, s101, 0
	global_load_dword v44, v178, s[100:101] nt
	s_add_u32 s100, s100, s89
	s_addc_u32 s101, s101, 0
	global_load_dword v45, v178, s[100:101] nt
	s_add_u32 s100, s100, s89
	s_addc_u32 s101, s101, 0
	global_load_dword v46, v178, s[100:101] nt
	s_add_u32 s100, s100, s89
	s_addc_u32 s101, s101, 0
	global_load_dword v47, v178, s[100:101] nt
	s_add_u32 s100, s100, s89
	s_addc_u32 s101, s101, 0
	global_load_dword v48, v178, s[100:101] nt
	s_add_u32 s100, s100, s89
	s_addc_u32 s101, s101, 0
	global_load_dword v49, v178, s[100:101] nt
	s_add_u32 s100, s100, s89
	s_addc_u32 s101, s101, 0
	global_load_dword v50, v178, s[100:101] nt
	s_add_u32 s100, s100, s89
	s_addc_u32 s101, s101, 0
	global_load_dword v51, v178, s[100:101] nt
	s_add_u32 s100, s100, s89
	s_addc_u32 s101, s101, 0
	global_load_dword v52, v178, s[100:101] nt
	s_add_u32 s100, s100, s89
	s_addc_u32 s101, s101, 0
	global_load_dword v53, v178, s[100:101] nt
	s_add_u32 s100, s100, s89
	s_addc_u32 s101, s101, 0
	global_load_dword v54, v178, s[100:101] nt
	s_add_u32 s100, s100, s89
	s_addc_u32 s101, s101, 0
	global_load_dword v55, v178, s[100:101] nt
	s_add_u32 s100, s100, s89
	s_addc_u32 s101, s101, 0
	global_load_dword v56, v178, s[100:101] nt
	s_add_u32 s100, s100, s89
	s_addc_u32 s101, s101, 0
	global_load_dword v57, v178, s[100:101] nt
	s_add_u32 s100, s100, s89
	s_addc_u32 s101, s101, 0
	global_load_dword v58, v178, s[100:101] nt
	s_add_u32 s100, s100, s89
	s_addc_u32 s101, s101, 0
	global_load_dword v59, v178, s[100:101] nt
	s_add_u32 s100, s100, s89
	s_addc_u32 s101, s101, 0
	global_load_dword v60, v178, s[100:101] nt
	s_add_u32 s100, s100, s89
	s_addc_u32 s101, s101, 0
	global_load_dword v61, v178, s[100:101] nt
	s_add_u32 s100, s100, s89
	s_addc_u32 s101, s101, 0
	global_load_dword v62, v178, s[100:101] nt
	s_add_u32 s100, s100, s89
	s_addc_u32 s101, s101, 0
	global_load_dword v63, v178, s[100:101] nt
	s_add_u32 s100, s100, s89
	s_addc_u32 s101, s101, 0
	global_load_dword v64, v178, s[100:101] nt
	s_add_u32 s100, s100, s89
	s_addc_u32 s101, s101, 0
	global_load_dword v65, v178, s[100:101] nt
	s_add_u32 s100, s100, s89
	s_addc_u32 s101, s101, 0
	global_load_dword v66, v178, s[100:101] nt
	s_add_u32 s100, s100, s89
	s_addc_u32 s101, s101, 0
	global_load_dword v67, v178, s[100:101] nt
	s_add_u32 s100, s100, s89
	s_addc_u32 s101, s101, 0
	global_load_dword v68, v178, s[100:101] nt
	s_add_u32 s100, s100, s89
	s_addc_u32 s101, s101, 0
	global_load_dword v69, v178, s[100:101] nt
	s_add_u32 s100, s100, s89
	s_addc_u32 s101, s101, 0
	global_load_dword v70, v178, s[100:101] nt
	s_add_u32 s100, s100, s89
	s_addc_u32 s101, s101, 0
	global_load_dword v71, v178, s[100:101] nt
	s_add_u32 s100, s100, s89
	s_addc_u32 s101, s101, 0
	global_load_dword v72, v178, s[100:101] nt
	s_add_u32 s100, s100, s89
	s_addc_u32 s101, s101, 0
	global_load_dword v73, v178, s[100:101] nt
	s_add_u32 s100, s100, s89
	s_addc_u32 s101, s101, 0
	global_load_dword v74, v178, s[100:101] nt
	s_add_u32 s100, s100, s89
	s_addc_u32 s101, s101, 0
	global_load_dword v75, v178, s[100:101] nt
	s_add_u32 s100, s100, s89
	s_addc_u32 s101, s101, 0
	global_load_dword v76, v178, s[100:101] nt
	s_add_u32 s100, s100, s89
	s_addc_u32 s101, s101, 0
	global_load_dword v77, v178, s[100:101] nt
	s_add_u32 s100, s100, s89
	s_addc_u32 s101, s101, 0
	global_load_dword v78, v178, s[100:101] nt
	s_add_u32 s100, s100, s89
	s_addc_u32 s101, s101, 0
	global_load_dword v79, v178, s[100:101] nt
	s_add_u32 s100, s100, s89
	s_addc_u32 s101, s101, 0
	global_load_dword v80, v178, s[100:101] nt
	s_add_u32 s100, s100, s89
	s_addc_u32 s101, s101, 0
	global_load_dword v81, v178, s[100:101] nt
	s_add_u32 s100, s100, s89
	s_addc_u32 s101, s101, 0
	global_load_dword v82, v178, s[100:101] nt
	s_add_u32 s100, s100, s89
	s_addc_u32 s101, s101, 0
	global_load_dword v83, v178, s[100:101] nt
	s_add_u32 s100, s100, s89
	s_addc_u32 s101, s101, 0
	global_load_dword v84, v178, s[100:101] nt
	s_add_u32 s100, s100, s89
	s_addc_u32 s101, s101, 0
	global_load_dword v85, v178, s[100:101] nt
	s_add_u32 s100, s100, s89
	s_addc_u32 s101, s101, 0
	global_load_dword v86, v178, s[100:101] nt
	s_add_u32 s100, s100, s89
	s_addc_u32 s101, s101, 0
	global_load_dword v87, v178, s[100:101] nt
	s_add_u32 s100, s100, s89
	s_addc_u32 s101, s101, 0
	global_load_dword v88, v178, s[100:101] nt
	s_add_u32 s100, s100, s89
	s_addc_u32 s101, s101, 0
	global_load_dword v89, v178, s[100:101] nt
	s_add_u32 s100, s100, s89
	s_addc_u32 s101, s101, 0
	global_load_dword v90, v178, s[100:101] nt
	s_add_u32 s100, s100, s89
	s_addc_u32 s101, s101, 0
	global_load_dword v91, v178, s[100:101] nt
	s_add_u32 s100, s100, s89
	s_addc_u32 s101, s101, 0
	global_load_dword v92, v178, s[100:101] nt
	s_add_u32 s100, s100, s89
	s_addc_u32 s101, s101, 0
	global_load_dword v93, v178, s[100:101] nt
	s_add_u32 s100, s100, s89
	s_addc_u32 s101, s101, 0
	global_load_dword v94, v178, s[100:101] nt
	s_add_u32 s100, s100, s89
	s_addc_u32 s101, s101, 0
	global_load_dword v95, v178, s[100:101] nt
	s_add_u32 s100, s100, s89
	s_addc_u32 s101, s101, 0
	global_load_dword v96, v178, s[100:101] nt
	s_add_u32 s100, s100, s89
	s_addc_u32 s101, s101, 0
	global_load_dword v97, v178, s[100:101] nt
	s_add_u32 s100, s100, s89
	s_addc_u32 s101, s101, 0
	s_waitcnt vmcnt(48)
	v_mul_f32_e32 v34, 0x42000000, v34
	v_mul_f32_e32 v35, 0x42000000, v35
	v_mul_f32_e32 v36, 0x42000000, v36
	v_mul_f32_e32 v37, 0x42000000, v37
	v_mul_f32_e32 v38, 0x42000000, v38
	v_mul_f32_e32 v39, 0x42000000, v39
	v_mul_f32_e32 v40, 0x42000000, v40
	v_mul_f32_e32 v41, 0x42000000, v41
	v_mul_f32_e32 v42, 0x42000000, v42
	v_mul_f32_e32 v43, 0x42000000, v43
	v_mul_f32_e32 v44, 0x42000000, v44
	v_mul_f32_e32 v45, 0x42000000, v45
	v_mul_f32_e32 v46, 0x42000000, v46
	v_mul_f32_e32 v47, 0x42000000, v47
	v_mul_f32_e32 v48, 0x42000000, v48
	v_mul_f32_e32 v49, 0x42000000, v49
	v_cvt_pk_fp8_f32 v154, v34, v35
	v_cvt_pk_fp8_f32 v155, v38, v39
	v_cvt_pk_fp8_f32 v156, v42, v43
	v_cvt_pk_fp8_f32 v157, v46, v47
	v_cvt_pk_fp8_f32 v154, v36, v37 op_sel:[0,0,1]
	v_cvt_pk_fp8_f32 v155, v40, v41 op_sel:[0,0,1]
	v_cvt_pk_fp8_f32 v156, v44, v45 op_sel:[0,0,1]
	v_cvt_pk_fp8_f32 v157, v48, v49 op_sel:[0,0,1]
	s_waitcnt vmcnt(32)
	v_mul_f32_e32 v50, 0x42000000, v50
	v_mul_f32_e32 v51, 0x42000000, v51
	v_mul_f32_e32 v52, 0x42000000, v52
	v_mul_f32_e32 v53, 0x42000000, v53
	v_mul_f32_e32 v54, 0x42000000, v54
	v_mul_f32_e32 v55, 0x42000000, v55
	v_mul_f32_e32 v56, 0x42000000, v56
	v_mul_f32_e32 v57, 0x42000000, v57
	v_mul_f32_e32 v58, 0x42000000, v58
	v_mul_f32_e32 v59, 0x42000000, v59
	v_mul_f32_e32 v60, 0x42000000, v60
	v_mul_f32_e32 v61, 0x42000000, v61
	v_mul_f32_e32 v62, 0x42000000, v62
	v_mul_f32_e32 v63, 0x42000000, v63
	v_mul_f32_e32 v64, 0x42000000, v64
	v_mul_f32_e32 v65, 0x42000000, v65
	v_cvt_pk_fp8_f32 v158, v50, v51
	v_cvt_pk_fp8_f32 v159, v54, v55
	v_cvt_pk_fp8_f32 v160, v58, v59
	v_cvt_pk_fp8_f32 v161, v62, v63
	v_cvt_pk_fp8_f32 v158, v52, v53 op_sel:[0,0,1]
	v_cvt_pk_fp8_f32 v159, v56, v57 op_sel:[0,0,1]
	v_cvt_pk_fp8_f32 v160, v60, v61 op_sel:[0,0,1]
	v_cvt_pk_fp8_f32 v161, v64, v65 op_sel:[0,0,1]
	s_waitcnt vmcnt(16)
	v_mul_f32_e32 v66, 0x42000000, v66
	v_mul_f32_e32 v67, 0x42000000, v67
	v_mul_f32_e32 v68, 0x42000000, v68
	v_mul_f32_e32 v69, 0x42000000, v69
	v_mul_f32_e32 v70, 0x42000000, v70
	v_mul_f32_e32 v71, 0x42000000, v71
	v_mul_f32_e32 v72, 0x42000000, v72
	v_mul_f32_e32 v73, 0x42000000, v73
	v_mul_f32_e32 v74, 0x42000000, v74
	v_mul_f32_e32 v75, 0x42000000, v75
	v_mul_f32_e32 v76, 0x42000000, v76
	v_mul_f32_e32 v77, 0x42000000, v77
	v_mul_f32_e32 v78, 0x42000000, v78
	v_mul_f32_e32 v79, 0x42000000, v79
	v_mul_f32_e32 v80, 0x42000000, v80
	v_mul_f32_e32 v81, 0x42000000, v81
	v_cvt_pk_fp8_f32 v162, v66, v67
	v_cvt_pk_fp8_f32 v163, v70, v71
	v_cvt_pk_fp8_f32 v164, v74, v75
	v_cvt_pk_fp8_f32 v165, v78, v79
	v_cvt_pk_fp8_f32 v162, v68, v69 op_sel:[0,0,1]
	v_cvt_pk_fp8_f32 v163, v72, v73 op_sel:[0,0,1]
	v_cvt_pk_fp8_f32 v164, v76, v77 op_sel:[0,0,1]
	v_cvt_pk_fp8_f32 v165, v80, v81 op_sel:[0,0,1]
	s_waitcnt vmcnt(0)
	v_mul_f32_e32 v82, 0x42000000, v82
	v_mul_f32_e32 v83, 0x42000000, v83
	v_mul_f32_e32 v84, 0x42000000, v84
	v_mul_f32_e32 v85, 0x42000000, v85
	v_mul_f32_e32 v86, 0x42000000, v86
	v_mul_f32_e32 v87, 0x42000000, v87
	v_mul_f32_e32 v88, 0x42000000, v88
	v_mul_f32_e32 v89, 0x42000000, v89
	v_mul_f32_e32 v90, 0x42000000, v90
	v_mul_f32_e32 v91, 0x42000000, v91
	v_mul_f32_e32 v92, 0x42000000, v92
	v_mul_f32_e32 v93, 0x42000000, v93
	v_mul_f32_e32 v94, 0x42000000, v94
	v_mul_f32_e32 v95, 0x42000000, v95
	v_mul_f32_e32 v96, 0x42000000, v96
	v_mul_f32_e32 v97, 0x42000000, v97
	v_cvt_pk_fp8_f32 v166, v82, v83
	v_cvt_pk_fp8_f32 v167, v86, v87
	v_cvt_pk_fp8_f32 v168, v90, v91
	v_cvt_pk_fp8_f32 v169, v94, v95
	v_cvt_pk_fp8_f32 v166, v84, v85 op_sel:[0,0,1]
	v_cvt_pk_fp8_f32 v167, v88, v89 op_sel:[0,0,1]
	v_cvt_pk_fp8_f32 v168, v92, v93 op_sel:[0,0,1]
	v_cvt_pk_fp8_f32 v169, v96, v97 op_sel:[0,0,1]
	s_mov_b32 vcc_lo, 0xaaaaaaaa
	s_mov_b32 vcc_hi, 0xaaaaaaaa
	s_nop 1
	v_cndmask_b32_dpp v170, v154, v158, vcc quad_perm:[1,0,3,2] row_mask:0xf bank_mask:0xf
	v_cndmask_b32_dpp v174, v162, v166, vcc quad_perm:[1,0,3,2] row_mask:0xf bank_mask:0xf
	v_cndmask_b32_dpp v171, v155, v159, vcc quad_perm:[1,0,3,2] row_mask:0xf bank_mask:0xf
	v_cndmask_b32_dpp v175, v163, v167, vcc quad_perm:[1,0,3,2] row_mask:0xf bank_mask:0xf
	v_cndmask_b32_dpp v172, v156, v160, vcc quad_perm:[1,0,3,2] row_mask:0xf bank_mask:0xf
	v_cndmask_b32_dpp v176, v164, v168, vcc quad_perm:[1,0,3,2] row_mask:0xf bank_mask:0xf
	v_cndmask_b32_dpp v173, v157, v161, vcc quad_perm:[1,0,3,2] row_mask:0xf bank_mask:0xf
	v_cndmask_b32_dpp v177, v165, v169, vcc quad_perm:[1,0,3,2] row_mask:0xf bank_mask:0xf
	s_mov_b32 vcc_lo, 0x55555555
	s_mov_b32 vcc_hi, 0x55555555
	s_nop 1
	v_cndmask_b32_dpp v154, v158, v154, vcc quad_perm:[1,0,3,2] row_mask:0xf bank_mask:0xf
	v_cndmask_b32_dpp v162, v166, v162, vcc quad_perm:[1,0,3,2] row_mask:0xf bank_mask:0xf
	v_cndmask_b32_dpp v155, v159, v155, vcc quad_perm:[1,0,3,2] row_mask:0xf bank_mask:0xf
	v_cndmask_b32_dpp v163, v167, v163, vcc quad_perm:[1,0,3,2] row_mask:0xf bank_mask:0xf
	v_cndmask_b32_dpp v156, v160, v156, vcc quad_perm:[1,0,3,2] row_mask:0xf bank_mask:0xf
	v_cndmask_b32_dpp v164, v168, v164, vcc quad_perm:[1,0,3,2] row_mask:0xf bank_mask:0xf
	v_cndmask_b32_dpp v157, v161, v157, vcc quad_perm:[1,0,3,2] row_mask:0xf bank_mask:0xf
	v_cndmask_b32_dpp v165, v169, v165, vcc quad_perm:[1,0,3,2] row_mask:0xf bank_mask:0xf
	s_mov_b32 vcc_lo, 0xcccccccc
	s_mov_b32 vcc_hi, 0xcccccccc
	s_nop 1
	v_cndmask_b32_dpp v158, v154, v162, vcc quad_perm:[2,3,0,1] row_mask:0xf bank_mask:0xf
	v_cndmask_b32_dpp v166, v170, v174, vcc quad_perm:[2,3,0,1] row_mask:0xf bank_mask:0xf
	v_cndmask_b32_dpp v159, v155, v163, vcc quad_perm:[2,3,0,1] row_mask:0xf bank_mask:0xf
	v_cndmask_b32_dpp v167, v171, v175, vcc quad_perm:[2,3,0,1] row_mask:0xf bank_mask:0xf
	v_cndmask_b32_dpp v160, v156, v164, vcc quad_perm:[2,3,0,1] row_mask:0xf bank_mask:0xf
	v_cndmask_b32_dpp v168, v172, v176, vcc quad_perm:[2,3,0,1] row_mask:0xf bank_mask:0xf
	v_cndmask_b32_dpp v161, v157, v165, vcc quad_perm:[2,3,0,1] row_mask:0xf bank_mask:0xf
	v_cndmask_b32_dpp v169, v173, v177, vcc quad_perm:[2,3,0,1] row_mask:0xf bank_mask:0xf
	s_mov_b32 vcc_lo, 0x33333333
	s_mov_b32 vcc_hi, 0x33333333
	s_nop 1
	v_cndmask_b32_dpp v154, v162, v154, vcc quad_perm:[2,3,0,1] row_mask:0xf bank_mask:0xf
	v_cndmask_b32_dpp v170, v174, v170, vcc quad_perm:[2,3,0,1] row_mask:0xf bank_mask:0xf
	v_cndmask_b32_dpp v155, v163, v155, vcc quad_perm:[2,3,0,1] row_mask:0xf bank_mask:0xf
	v_cndmask_b32_dpp v171, v175, v171, vcc quad_perm:[2,3,0,1] row_mask:0xf bank_mask:0xf
	v_cndmask_b32_dpp v156, v164, v156, vcc quad_perm:[2,3,0,1] row_mask:0xf bank_mask:0xf
	v_cndmask_b32_dpp v172, v176, v172, vcc quad_perm:[2,3,0,1] row_mask:0xf bank_mask:0xf
	v_cndmask_b32_dpp v157, v165, v157, vcc quad_perm:[2,3,0,1] row_mask:0xf bank_mask:0xf
	v_cndmask_b32_dpp v173, v177, v173, vcc quad_perm:[2,3,0,1] row_mask:0xf bank_mask:0xf
	global_store_dwordx4 v179, v[154:157], s[82:83] nt
	global_store_dwordx4 v180, v[170:173], s[82:83] nt
	global_store_dwordx4 v181, v[158:161], s[82:83] nt
	global_store_dwordx4 v190, v[166:169], s[82:83] nt
	s_lshl_b32 s2, s74, 3
	s_add_i32 s98, s98, s2
	s_cmp_gt_u32 s98, 26623
	s_cbranch_scc1 .Lhw_seam0_done
	v_mbcnt_lo_u32_b32 v178, -1, 0
	v_mbcnt_hi_u32_b32 v178, -1, v178
	v_and_b32_e32 v179, 60, v178
	v_lshlrev_b32_e32 v179, 10, v179
	v_and_b32_e32 v180, 3, v178
	v_lshl_or_b32 v179, v180, 4, v179
	v_add_u32_e32 v180, 0x400, v179
	v_add_u32_e32 v181, 0x800, v179
	v_add_u32_e32 v190, 0xc00, v179
	v_lshlrev_b32_e32 v178, 2, v178
	s_sub_i32 s2, s98, 2048
	s_cmp_lt_u32 s2, 16384
	s_cbranch_scc0 .Lhw_dn_s0_1
	s_lshr_b32 s9, s2, 9
	s_bfe_u32 s32, s2, 0x40005
	s_and_b32 s53, s2, 31
	s_lshl_b32 s69, s9, 23
	s_lshl_b32 s100, s32, 19
	s_add_i32 s69, s69, s100
	s_lshl_b32 s100, s53, 8
	s_add_i32 s69, s69, s100
	s_lshl_b32 s99, s9, 11
	s_bfe_u32 s100, s53, 0x30001
	s_lshl_b32 s100, s100, 8
	s_add_i32 s99, s99, s100
	s_lshr_b32 s100, s53, 4
	s_lshl_b32 s100, s100, 7
	s_add_i32 s99, s99, s100
	s_and_b32 s100, s53, 1
	s_lshl_b32 s100, s100, 6
	s_add_i32 s99, s99, s100
	s_lshl_b32 s99, s99, 10
	s_lshl_b32 s100, s32, 6
	s_add_i32 s99, s99, s100
	s_add_i32 s99, s99, 0x2000000
	v_readlane_b32 s82, v239, 11
	v_readlane_b32 s83, v239, 12
	s_movk_i32 s89, 8192
	s_branch .Lhw_go_s0_1
